# warm2
# baseline (speedup 1.0000x reference)
_Z11prep_kernelPKfS0_PKiS2_S0_S0_S0_S0_S0_S0_Pc:
	s_getpc_b64 s[36:37]
	s_add_u32 s38, s36, _Z11attn_kernelILi4EEvPKfS1_S1_S1_S1_S1_PKcPf@rel32@lo+4
	s_addc_u32 s39, s37, _Z11attn_kernelILi4EEvPKfS1_S1_S1_S1_S1_PKcPf@rel32@hi+12
	v_and_b32_e32 v192, 63, v0
	v_lshlrev_b32_e32 v192, 7, v192
	v_min_u32_e32 v193, 0x980, v192
	v_min_u32_e32 v192, 0x1180, v192
	global_load_dword v193, v193, s[36:37] offset:-4
	global_load_dword v192, v192, s[38:39]
	s_lshr_b32 s4, s2, 2
	v_lshrrev_b32_e32 v2, 6, v0
	s_and_b32 s4, s4, 0x1ffffffe
	s_load_dwordx4 s[28:31], s[0:1], 0x40
	s_load_dwordx8 s[12:19], s[0:1], 0x0
	s_load_dwordx8 s[20:27], s[0:1], 0x20
	s_load_dwordx2 s[32:33], s[0:1], 0x50
	v_and_b32_e32 v1, 15, v0
	s_and_b32 s3, s2, 7
	v_or_b32_e32 v2, s4, v2
	v_lshl_or_b32 v88, v2, 3, s3
	v_cmp_gt_u32_e64 s[10:11], 14, v1
	v_mul_lo_u32 v7, v88, 14
	v_and_b32_e32 v105, 63, v0
	v_cndmask_b32_e64 v6, 13, v1, s[10:11]
	v_add_u32_e32 v2, v7, v6
	v_mul_u32_u24_e32 v4, 12, v2
	v_lshlrev_b32_e32 v5, 2, v6
	v_cmp_gt_u32_e64 s[8:9], 48, v105
	v_cmp_gt_u32_e64 s[6:7], 14, v105
	v_lshlrev_b32_e32 v118, 1, v0
	v_lshrrev_b32_e32 v104, 4, v0
	v_cndmask_b32_e64 v8, 0, v105, s[8:9]
	v_cndmask_b32_e64 v9, 0, v105, s[6:7]
	v_mad_u32_u24 v8, v88, 48, v8
	v_add_lshl_u32 v9, v7, v9, 2
	v_lshlrev_b32_e32 v8, 2, v8
	s_lshl_b32 s2, s2, 3
	s_and_b32 s2, s2, 0x78
	v_and_b32_e32 v106, 30, v118
	v_or_b32_e32 v107, s2, v104
	v_cmp_gt_u32_e64 s[2:3], 23, v106
	v_or_b32_e32 v10, 1, v106
	v_cmp_gt_u32_e64 s[4:5], 23, v10
	v_lshlrev_b32_e32 v11, 7, v106
	v_lshlrev_b32_e32 v10, 7, v10
	v_cndmask_b32_e64 v11, 0, v11, s[2:3]
	v_cndmask_b32_e64 v10, 0, v10, s[4:5]
	v_or_b32_e32 v11, v11, v107
	v_or_b32_e32 v10, v10, v107
	v_lshlrev_b32_e32 v11, 2, v11
	v_lshlrev_b32_e32 v10, 2, v10
	v_lshlrev_b32_e32 v12, 2, v107
	v_lshlrev_b32_e32 v119, 5, v0
	v_lshlrev_b32_e32 v13, 2, v0
	v_and_b32_e32 v109, 12, v13
	v_and_b32_e32 v91, 0xf80, v119
	v_lshl_or_b32 v91, v109, 2, v91
	v_or_b32_e32 v92, 0x1000, v91
	v_lshlrev_b32_e32 v90, 9, v2
	v_and_b32_e32 v16, 48, v0
	v_or_b32_e32 v90, v90, v16
	v_or_b32_e32 v112, 0x80, v0
	v_or_b32_e32 v111, 0x180, v0
	v_or_b32_e32 v108, 0x280, v0
	v_mov_b32_e32 v87, 0
	v_bfe_u32 v110, v0, 4, 2
	s_movk_i32 s34, 0x60
	v_lshrrev_b32_e32 v136, 1, v0
	v_lshrrev_b32_e32 v18, 3, v0
	v_and_b32_e32 v18, 4, v18
	v_and_b32_e32 v19, 24, v0
	v_and_b32_e32 v20, 2, v136
	v_or3_b32 v18, v18, v19, v20
	v_and_or_b32 v136, v136, s34, v18
	v_mul_u32_u24_e32 v18, 0x110, v109
	v_lshl_add_u32 v136, v136, 1, v18
	v_add_u32_e32 v137, 0x1100, v136
	v_add_u32_e32 v138, 0x2200, v136
	v_lshlrev_b32_e32 v18, 9, v88
	v_and_b32_e32 v19, 0x100, v119
	v_lshlrev_b32_e32 v20, 4, v0
	v_and_b32_e32 v20, 48, v20
	v_or3_b32 v139, v18, v19, v20
	v_and_b32_e32 v19, 8, v118
	v_and_b32_e32 v20, 64, v118
	v_or3_b32 v139, v139, v19, v20
	v_lshlrev_b32_e32 v19, 2, v110
	v_and_b32_e32 v20, 4, v19
	v_or_b32_e32 v139, v139, v20
	v_lshl_or_b32 v140, v1, 5, v18
	v_or_b32_e32 v140, v140, v19
	v_add_u32_e32 v140, 0x80000, v140
	v_lshl_or_b32 v141, v88, 4, v1
	v_lshlrev_b32_e32 v141, 3, v141
	v_add_u32_e32 v141, 0x140000, v141
	v_lshlrev_b32_e32 v20, 8, v88
	v_mul_u32_u24_e32 v21, 43, v105
	v_lshrrev_b32_e32 v21, 9, v21
	v_mul_u32_u24_e32 v21, 12, v21
	v_sub_u32_e32 v22, v105, v21
	v_and_b32_e32 v142, 3, v22
	v_lshrrev_b32_e32 v22, 2, v22
	v_mad_u32_u24 v142, v142, 3, v22
	v_add_u32_e32 v142, v142, v21
	v_lshl_add_u32 v142, v142, 2, v20
	v_add_u32_e32 v142, 0x164000, v142
	v_lshl_add_u32 v143, v105, 2, v20
	v_add_u32_e32 v143, 0x164000, v143
	v_lshlrev_b32_e32 v123, 6, v107
	v_lshl_add_u32 v123, v106, 1, v123
	v_add_u32_e32 v123, 0x160000, v123
	v_lshl_add_u32 v122, v1, 4, v20
	v_or_b32_e32 v122, v122, v19
	v_add_u32_e32 v122, 0x100000, v122
	s_waitcnt lgkmcnt(0)
	global_load_dwordx3 v[82:84], v4, s[12:13]
	global_load_dword v85, v5, s[26:27]
	global_load_dword v114, v8, s[18:19]
	global_load_dword v115, v9, s[16:17]
	global_load_dword v116, v11, s[28:29]
	global_load_dword v113, v10, s[28:29]
	global_load_dword v117, v12, s[30:31]
	global_load_dwordx4 v[66:69], v91, s[20:21]
	global_load_dwordx4 v[70:73], v91, s[20:21] offset:64
	global_load_dwordx4 v[74:77], v92, s[20:21]
	global_load_dwordx4 v[78:81], v92, s[20:21] offset:64
	global_load_dwordx4 v[58:61], v91, s[22:23]
	global_load_dwordx4 v[62:65], v91, s[22:23] offset:64
	global_load_dwordx4 v[50:53], v92, s[22:23]
	global_load_dwordx4 v[54:57], v92, s[22:23] offset:64
	global_load_dwordx4 v[42:45], v91, s[24:25]
	global_load_dwordx4 v[46:49], v91, s[24:25] offset:64
	global_load_dwordx4 v[34:37], v92, s[24:25]
	global_load_dwordx4 v[38:41], v92, s[24:25] offset:64
	global_load_dwordx4 v[26:29], v90, s[14:15] nt
	global_load_dwordx4 v[30:33], v90, s[14:15] offset:64 nt
	global_load_dwordx4 v[18:21], v90, s[14:15] offset:128 nt
	global_load_dwordx4 v[22:25], v90, s[14:15] offset:192 nt
	global_load_dwordx4 v[10:13], v90, s[14:15] offset:256 nt
	global_load_dwordx4 v[14:17], v90, s[14:15] offset:320 nt
	global_load_dwordx4 v[2:5], v90, s[14:15] offset:384 nt
	global_load_dwordx4 v[6:9], v90, s[14:15] offset:448 nt
	s_waitcnt vmcnt(26)
	v_mov_b32_e32 v90, v83
	v_mov_b32_e32 v91, v84
	v_lshlrev_b32_e32 v86, 2, v110
	s_waitcnt vmcnt(25)
	v_mul_f32_e32 v84, 0x3fb8aa3b, v85
	s_mov_b32 s14, 0x41700000
	v_exp_f32_e32 v84, v84
	v_cndmask_b32_e64 v94, 0, 1.0, s[10:11]
	v_add_f32_e32 v84, 1.0, v84
	v_cmp_lt_f32_e32 vcc, s14, v85
	v_log_f32_e32 v84, v84
	v_cmp_lt_u32_e64 s[12:13], 15, v105
	v_mul_f32_e32 v84, 0x3f317218, v84
	v_cndmask_b32_e32 v84, v84, v85, vcc
	v_mul_f32_e32 v84, 0xbe715bef, v84
	v_mul_f32_e32 v84, 0x3f3504f3, v84
	v_mul_f32_e32 v84, 0x41800000, v84
	v_cndmask_b32_e64 v99, 0, v84, s[10:11]
	v_mul_f32_e32 v101, -2.0, v99
	v_mul_f32_e32 v100, v82, v82
	v_cmp_gt_u32_e32 vcc, 16, v105
	v_fmac_f32_e32 v100, v90, v90
	v_cmp_eq_u32_e64 s[12:13], 0, v110
	v_fmac_f32_e32 v100, v91, v91
	v_cmp_eq_u32_e64 s[14:15], 1, v110
	v_mul_f32_e32 v83, v101, v82
	v_cmp_eq_u32_e64 s[16:17], 2, v110
	v_mul_f32_e32 v84, v101, v90
	v_mul_f32_e32 v85, v101, v91
	v_mul_f32_e32 v89, v99, v100
	v_mul_f32_e32 v92, v82, v94
	v_mul_f32_e32 v93, v90, v94
	v_mul_f32_e32 v95, v91, v94
	v_mul_f32_e32 v96, v100, v94
	v_cvt_pk_fp8_f32 v88, v83, v83
	v_cvt_pk_fp8_f32 v104, v84, v84
	v_cvt_f32_fp8_e32 v97, v88
	v_cvt_f32_fp8_e32 v98, v104
	v_sub_f32_e32 v97, v83, v97
	v_sub_f32_e32 v98, v84, v98
	v_cvt_pk_fp8_f32 v88, v85, v85
	v_cvt_pk_fp8_f32 v104, v99, v99
	v_cvt_f32_fp8_e32 v101, v88
	v_cvt_f32_fp8_e32 v102, v104
	v_sub_f32_e32 v101, v85, v101
	v_sub_f32_e32 v102, v99, v102
	v_cvt_pk_fp8_f32 v88, v89, v89
	v_cvt_pk_fp8_f32 v104, v92, v92
	v_cvt_f32_fp8_e32 v103, v88
	v_cvt_f32_fp8_e32 v120, v104
	v_sub_f32_e32 v103, v89, v103
	v_sub_f32_e32 v120, v92, v120
	v_cvt_pk_fp8_f32 v88, v93, v93
	v_cvt_pk_fp8_f32 v104, v95, v95
	v_cvt_f32_fp8_e32 v121, v88
	v_cvt_f32_fp8_e32 v86, v104
	v_sub_f32_e32 v121, v93, v121
	v_sub_f32_e32 v86, v95, v86
	v_cvt_pk_fp8_f32 v88, v96, v96
	s_nop 0
	v_cvt_f32_fp8_e32 v87, v88
	s_nop 0
	v_sub_f32_e32 v87, v96, v87
	v_cndmask_b32_e64 v124, v89, v85, s[16:17]
	v_cndmask_b32_e64 v124, v124, v98, s[14:15]
	v_cndmask_b32_e64 v124, v124, v83, s[12:13]
	v_cndmask_b32_e64 v125, v103, v99, s[16:17]
	v_cndmask_b32_e64 v125, v125, v84, s[14:15]
	v_cndmask_b32_e64 v125, v125, v97, s[12:13]
	v_cndmask_b32_e64 v126, 0, v102, s[16:17]
	v_cndmask_b32_e64 v126, v126, v85, s[14:15]
	v_cndmask_b32_e64 v126, v126, v83, s[12:13]
	v_cndmask_b32_e64 v127, 0, v99, s[16:17]
	v_cndmask_b32_e64 v127, v127, v101, s[14:15]
	v_cndmask_b32_e64 v127, v127, v84, s[12:13]
	v_cndmask_b32_e64 v128, v94, v86, s[16:17]
	v_cndmask_b32_e64 v128, v128, v93, s[14:15]
	v_cndmask_b32_e64 v128, v128, v92, s[12:13]
	v_cndmask_b32_e64 v129, v94, v96, s[16:17]
	v_cndmask_b32_e64 v129, v129, v121, s[14:15]
	v_cndmask_b32_e64 v129, v129, v92, s[12:13]
	v_cndmask_b32_e64 v130, 0, v96, s[16:17]
	v_cndmask_b32_e64 v130, v130, v95, s[14:15]
	v_cndmask_b32_e64 v130, v130, v120, s[12:13]
	v_cndmask_b32_e64 v131, 0, v87, s[16:17]
	v_cndmask_b32_e64 v131, v131, v95, s[14:15]
	v_cndmask_b32_e64 v131, v131, v93, s[12:13]
	v_cvt_pk_fp8_f32 v119, v124, v125
	v_cvt_pk_fp8_f32 v103, v128, v129
	v_cvt_pk_fp8_f32 v119, v126, v127 op_sel:[0,0,1]
	v_cvt_pk_fp8_f32 v103, v130, v131 op_sel:[0,0,1]
	s_nop 0
	global_store_dword v139, v119, s[32:33] offset:128
	global_store_dword v140, v103, s[32:33] offset:16
	s_and_saveexec_b64 s[0:1], vcc
	s_cbranch_execz .LBB0_14
	v_cvt_f16_f32_e32 v83, v82
	v_cvt_pk_f16_f32 v90, v90, v91
	s_nop 0
	v_alignbit_b32 v91, 0, v90, 16
	v_pack_b32_f16 v90, v83, v90
	global_store_dwordx2 v141, v[90:91], s[32:33]
